# v38
# baseline (speedup 1.0000x reference)
.LBB3_145:
	s_or_b64 exec, exec, s[54:55]
	v_div_scale_f32 v171, s[54:55], v163, v163, 1.0
	v_rcp_f32_e32 v197, v171
	v_div_scale_f32 v201, vcc, 1.0, v163, 1.0
	s_movk_i32 s69, 0x410
	v_fma_f32 v202, -v171, v197, 1.0
	v_fmac_f32_e32 v197, v202, v197
	v_mul_f32_e32 v202, v201, v197
	v_fma_f32 v203, -v171, v202, v201
	v_fmac_f32_e32 v202, v203, v197
	v_fma_f32 v171, -v171, v202, v201
	v_div_fmas_f32 v171, v171, v197, v202
	v_lshlrev_b32_e32 v197, 6, v189
	v_div_fixup_f32 v171, v171, v163, 1.0
	v_cmp_lt_f32_e32 vcc, 0, v163
	v_mul_lo_u32 v169, v169, s69
	v_and_b32_e32 v197, 0x3c0, v197
	v_cndmask_b32_e32 v163, 0, v171, vcc
	v_sub_u32_e32 v171, v160, v168
	v_add3_u32 v201, s99, v169, v197
	s_max_i32 s54, s33, s96
	s_max_i32 s55, s97, s75
	s_max_i32 s54, s54, s55
	s_cmp_gt_i32 s54, 32
	s_cbranch_scc1 .Lww_slow
	v_lshl_add_u32 v202, v171, 1, v201
	s_and_saveexec_b64 s[54:55], s[44:45]
	s_cbranch_execz .Lww_s1
	v_fma_mixlo_f16 v203, v163, v225, 0
	ds_write_b16 v202, v203
.Lww_s1:
	s_or_b64 exec, exec, s[54:55]
	s_and_saveexec_b64 s[54:55], s[50:51]
	s_cbranch_execz .Lww_s2
	v_fma_mixlo_f16 v203, v163, v224, 0
	ds_write_b16 v202, v203 offset:2
.Lww_s2:
	s_or_b64 exec, exec, s[54:55]
	s_and_saveexec_b64 s[54:55], s[48:49]
	s_cbranch_execz .Lww_s3
	v_fma_mixlo_f16 v203, v163, v223, 0
	ds_write_b16 v202, v203 offset:4
.Lww_s3:
	s_or_b64 exec, exec, s[54:55]
	s_and_saveexec_b64 s[54:55], s[46:47]
	s_cbranch_execz .Lww_s4
	v_fma_mixlo_f16 v203, v163, v222, 0
	ds_write_b16 v202, v203 offset:6
.Lww_s4:
	s_or_b64 exec, exec, s[54:55]
	s_and_saveexec_b64 s[54:55], s[42:43]
	s_cbranch_execz .Lww_s5
	v_fma_mixlo_f16 v203, v163, v221, 0
	ds_write_b16 v202, v203 offset:8
.Lww_s5:
	s_or_b64 exec, exec, s[54:55]
	s_and_saveexec_b64 s[54:55], s[40:41]
	s_cbranch_execz .Lww_s6
	v_fma_mixlo_f16 v203, v163, v220, 0
	ds_write_b16 v202, v203 offset:10
.Lww_s6:
	s_or_b64 exec, exec, s[54:55]
	s_and_saveexec_b64 s[54:55], s[38:39]
	s_cbranch_execz .Lww_s7
	v_fma_mixlo_f16 v203, v163, v219, 0
	ds_write_b16 v202, v203 offset:12
.Lww_s7:
	s_or_b64 exec, exec, s[54:55]
	s_and_saveexec_b64 s[54:55], s[36:37]
	s_cbranch_execz .Lww_s8
	v_fma_mixlo_f16 v203, v163, v218, 0
	ds_write_b16 v202, v203 offset:14
.Lww_s8:
	s_or_b64 exec, exec, s[54:55]
	s_and_saveexec_b64 s[54:55], s[34:35]
	s_cbranch_execz .Lww_s9
	v_fma_mixlo_f16 v203, v163, v217, 0
	ds_write_b16 v202, v203 offset:16
.Lww_s9:
	s_or_b64 exec, exec, s[54:55]
	s_and_saveexec_b64 s[54:55], s[30:31]
	s_cbranch_execz .Lww_s10
	v_fma_mixlo_f16 v203, v163, v216, 0
	ds_write_b16 v202, v203 offset:18
.Lww_s10:
	s_or_b64 exec, exec, s[54:55]
	s_and_saveexec_b64 s[54:55], s[28:29]
	s_cbranch_execz .Lww_s11
	v_fma_mixlo_f16 v203, v163, v215, 0
	ds_write_b16 v202, v203 offset:20
.Lww_s11:
	s_or_b64 exec, exec, s[54:55]
	s_and_saveexec_b64 s[54:55], s[26:27]
	s_cbranch_execz .Lww_s12
	v_fma_mixlo_f16 v203, v163, v214, 0
	ds_write_b16 v202, v203 offset:22
.Lww_s12:
	s_or_b64 exec, exec, s[54:55]
	s_and_saveexec_b64 s[54:55], s[24:25]
	s_cbranch_execz .Lww_s13
	v_fma_mixlo_f16 v203, v163, v200, 0
	ds_write_b16 v202, v203 offset:24
.Lww_s13:
	s_or_b64 exec, exec, s[54:55]
	s_and_saveexec_b64 s[54:55], s[22:23]
	s_cbranch_execz .Lww_s14
	v_fma_mixlo_f16 v203, v163, v199, 0
	ds_write_b16 v202, v203 offset:26
.Lww_s14:
	s_or_b64 exec, exec, s[54:55]
	s_and_saveexec_b64 s[54:55], s[20:21]
	s_cbranch_execz .Lww_s15
	v_fma_mixlo_f16 v203, v163, v198, 0
	ds_write_b16 v202, v203 offset:28
.Lww_s15:
	s_or_b64 exec, exec, s[54:55]
	s_and_saveexec_b64 s[54:55], s[18:19]
	s_cbranch_execz .Lww_s16
	v_fma_mixlo_f16 v203, v163, v196, 0
	ds_write_b16 v202, v203 offset:30
.Lww_s16:
	s_or_b64 exec, exec, s[54:55]
	s_and_saveexec_b64 s[54:55], s[16:17]
	s_cbranch_execz .Lww_s17
	v_fma_mixlo_f16 v203, v163, v195, 0
	ds_write_b16 v202, v203 offset:32
.Lww_s17:
	s_or_b64 exec, exec, s[54:55]
	s_and_saveexec_b64 s[54:55], s[14:15]
	s_cbranch_execz .Lww_s18
	v_fma_mixlo_f16 v203, v163, v176, 0
	ds_write_b16 v202, v203 offset:34
.Lww_s18:
	s_or_b64 exec, exec, s[54:55]
	s_and_saveexec_b64 s[54:55], s[12:13]
	s_cbranch_execz .Lww_s19
	v_fma_mixlo_f16 v203, v163, v175, 0
	ds_write_b16 v202, v203 offset:36
.Lww_s19:
	s_or_b64 exec, exec, s[54:55]
	s_and_saveexec_b64 s[54:55], s[10:11]
	s_cbranch_execz .Lww_s20
	v_fma_mixlo_f16 v203, v163, v174, 0
	ds_write_b16 v202, v203 offset:38
.Lww_s20:
	s_or_b64 exec, exec, s[54:55]
	s_and_saveexec_b64 s[54:55], s[8:9]
	s_cbranch_execz .Lww_s21
	v_fma_mixlo_f16 v203, v163, v173, 0
	ds_write_b16 v202, v203 offset:40
.Lww_s21:
	s_or_b64 exec, exec, s[54:55]
	s_and_saveexec_b64 s[54:55], s[6:7]
	s_cbranch_execz .Lww_s22
	v_fma_mixlo_f16 v203, v163, v172, 0
	ds_write_b16 v202, v203 offset:42
.Lww_s22:
	s_or_b64 exec, exec, s[54:55]
	s_and_saveexec_b64 s[54:55], s[4:5]
	s_cbranch_execz .Lww_s23
	v_fma_mixlo_f16 v203, v163, v164, 0
	ds_write_b16 v202, v203 offset:44
.Lww_s23:
	s_or_b64 exec, exec, s[54:55]
	s_and_saveexec_b64 s[54:55], s[52:53]
	s_cbranch_execz .Lww_s24
	v_fma_mixlo_f16 v203, v163, v161, 0
	ds_write_b16 v202, v203 offset:46
.Lww_s24:
	s_or_b64 exec, exec, s[54:55]
	s_and_saveexec_b64 s[4:5], s[0:1]
	s_cbranch_execnz .LBB3_194
	s_branch .LBB3_196
.Lww_slow:
	s_and_saveexec_b64 s[54:55], s[44:45]
	s_cbranch_execnz .LBB3_170
	s_or_b64 exec, exec, s[54:55]
	s_and_saveexec_b64 s[44:45], s[50:51]
	s_cbranch_execnz .LBB3_171
